# MoE tile table built by scalar code in every wave (prefix, XCD flags, unit slots; tiles ordered full first, smallest last) instead of one-lane serial block
# baseline (speedup 1.0000x reference)
; __global__ void __launch_bounds__(512, 2) hymba_fwd(Args args) {
;     ...
;         if (tid < NEXP) tb[33 + tid] = (int)__hip_atomic_load((unsigned*)(ctl + CW_CNT + 64 * tid), RLX_AGENT);
;         __syncthreads();
;         if (tid == 0) { int acc = 0; for (int e = 0; e < NEXP; ++e) { const int c = tb[33 + e]; tb[e] = acc; acc += (c + 255) >> 8; } tb[32] = acc;
;             int ok = (G == 256) ? 1 : 0, F = 0, rank = 0, mine = 0; const int x = bx & 7, j = bx >> 3;
;             for (int xx = 0; xx < 8; ++xx) { int tx = 0; for (int k = 0; k < 4; ++k) tx += tb[xx + 8 * k + 1] - tb[xx + 8 * k]; if (tx > 12) ok = 0;
;                 int f = 8 * tx - 64; f = f < 0 ? 0 : (f > 32 ? 32 : f);
;                 F += 32 - f; int below = j + (xx < x ? 1 : 0) - f; below = below < 0 ? 0 : (below > 32 - f ? 32 - f : below); rank += below; if (xx == x) mine = (j >= f) ? 1 : 0; }
;             tb[66] = ok; tb[67] = F; tb[68] = mine ? rank : -1;
.LBB0_677:
	s_or_b64 exec, exec, s[0:1]
	v_cmp_eq_u32_e32 vcc, 0, v28
	s_waitcnt lgkmcnt(0)
	s_barrier
	v_mbcnt_lo_u32_b32 v1, -1, 0
	v_mbcnt_hi_u32_b32 v1, -1, v1
	v_lshlrev_b32_e32 v2, 2, v1
	v_add_u32_e32 v2, 0x22400, v2
	ds_read_b32 v3, v2 offset:132
	v_cmp_gt_u32_e32 vcc, 32, v1
	s_waitcnt lgkmcnt(0)
	v_cndmask_b32_e32 v3, 0, v3, vcc
	v_add_u32_e32 v4, 0xff, v3
	v_lshrrev_b32_e32 v4, 8, v4
	v_mov_b32_e32 v5, 0
	s_mov_b32 s6, 0
	s_nop 0
	v_readlane_b32 s7, v4, 0
	v_writelane_b32 v5, s6, 0
	s_add_i32 s6, s6, s7
	v_readlane_b32 s7, v4, 1
	v_writelane_b32 v5, s6, 1
	s_add_i32 s6, s6, s7
	v_readlane_b32 s7, v4, 2
	v_writelane_b32 v5, s6, 2
	s_add_i32 s6, s6, s7
	v_readlane_b32 s7, v4, 3
	v_writelane_b32 v5, s6, 3
	s_add_i32 s6, s6, s7
	v_readlane_b32 s7, v4, 4
	v_writelane_b32 v5, s6, 4
	s_add_i32 s6, s6, s7
	v_readlane_b32 s7, v4, 5
	v_writelane_b32 v5, s6, 5
	s_add_i32 s6, s6, s7
	v_readlane_b32 s7, v4, 6
	v_writelane_b32 v5, s6, 6
	s_add_i32 s6, s6, s7
	v_readlane_b32 s7, v4, 7
	v_writelane_b32 v5, s6, 7
	s_add_i32 s6, s6, s7
	v_readlane_b32 s7, v4, 8
	v_writelane_b32 v5, s6, 8
	s_add_i32 s6, s6, s7
	v_readlane_b32 s7, v4, 9
	v_writelane_b32 v5, s6, 9
	s_add_i32 s6, s6, s7
	v_readlane_b32 s7, v4, 10
	v_writelane_b32 v5, s6, 10
	s_add_i32 s6, s6, s7
	v_readlane_b32 s7, v4, 11
	v_writelane_b32 v5, s6, 11
	s_add_i32 s6, s6, s7
	v_readlane_b32 s7, v4, 12
	v_writelane_b32 v5, s6, 12
	s_add_i32 s6, s6, s7
	v_readlane_b32 s7, v4, 13
	v_writelane_b32 v5, s6, 13
	s_add_i32 s6, s6, s7
	v_readlane_b32 s7, v4, 14
	v_writelane_b32 v5, s6, 14
	s_add_i32 s6, s6, s7
	v_readlane_b32 s7, v4, 15
	v_writelane_b32 v5, s6, 15
	s_add_i32 s6, s6, s7
	v_readlane_b32 s7, v4, 16
	v_writelane_b32 v5, s6, 16
	s_add_i32 s6, s6, s7
	v_readlane_b32 s7, v4, 17
	v_writelane_b32 v5, s6, 17
	s_add_i32 s6, s6, s7
	v_readlane_b32 s7, v4, 18
	v_writelane_b32 v5, s6, 18
	s_add_i32 s6, s6, s7
	v_readlane_b32 s7, v4, 19
	v_writelane_b32 v5, s6, 19
	s_add_i32 s6, s6, s7
	v_readlane_b32 s7, v4, 20
	v_writelane_b32 v5, s6, 20
	s_add_i32 s6, s6, s7
	v_readlane_b32 s7, v4, 21
	v_writelane_b32 v5, s6, 21
	s_add_i32 s6, s6, s7
	v_readlane_b32 s7, v4, 22
	v_writelane_b32 v5, s6, 22
	s_add_i32 s6, s6, s7
	v_readlane_b32 s7, v4, 23
	v_writelane_b32 v5, s6, 23
	s_add_i32 s6, s6, s7
	v_readlane_b32 s7, v4, 24
	v_writelane_b32 v5, s6, 24
	s_add_i32 s6, s6, s7
	v_readlane_b32 s7, v4, 25
	v_writelane_b32 v5, s6, 25
	s_add_i32 s6, s6, s7
	v_readlane_b32 s7, v4, 26
	v_writelane_b32 v5, s6, 26
	s_add_i32 s6, s6, s7
	v_readlane_b32 s7, v4, 27
	v_writelane_b32 v5, s6, 27
	s_add_i32 s6, s6, s7
	v_readlane_b32 s7, v4, 28
	v_writelane_b32 v5, s6, 28
	s_add_i32 s6, s6, s7
	v_readlane_b32 s7, v4, 29
	v_writelane_b32 v5, s6, 29
	s_add_i32 s6, s6, s7
	v_readlane_b32 s7, v4, 30
	v_writelane_b32 v5, s6, 30
	s_add_i32 s6, s6, s7
	v_readlane_b32 s7, v4, 31
	v_writelane_b32 v5, s6, 31
	s_add_i32 s6, s6, s7
	v_writelane_b32 v5, s6, 32
	v_cmp_gt_u32_e32 vcc, 33, v1
	s_and_saveexec_b64 s[10:11], vcc
	ds_write_b32 v2, v5
	s_or_b64 exec, exec, s[10:11]
	v_readlane_b32 s40, v4, 0
	v_readlane_b32 s10, v4, 8
	v_readlane_b32 s11, v4, 16
	v_readlane_b32 s12, v4, 24
	s_add_i32 s40, s40, s10
	s_add_i32 s40, s40, s11
	s_add_i32 s40, s40, s12
	v_readlane_b32 s41, v4, 1
	v_readlane_b32 s10, v4, 9
	v_readlane_b32 s11, v4, 17
	v_readlane_b32 s12, v4, 25
	s_add_i32 s41, s41, s10
	s_add_i32 s41, s41, s11
	s_add_i32 s41, s41, s12
	v_readlane_b32 s42, v4, 2
	v_readlane_b32 s10, v4, 10
	v_readlane_b32 s11, v4, 18
	v_readlane_b32 s12, v4, 26
	s_add_i32 s42, s42, s10
	s_add_i32 s42, s42, s11
	s_add_i32 s42, s42, s12
	v_readlane_b32 s43, v4, 3
	v_readlane_b32 s10, v4, 11
	v_readlane_b32 s11, v4, 19
	v_readlane_b32 s12, v4, 27
	s_add_i32 s43, s43, s10
	s_add_i32 s43, s43, s11
	s_add_i32 s43, s43, s12
	v_readlane_b32 s44, v4, 4
	v_readlane_b32 s10, v4, 12
	v_readlane_b32 s11, v4, 20
	v_readlane_b32 s12, v4, 28
	s_add_i32 s44, s44, s10
	s_add_i32 s44, s44, s11
	s_add_i32 s44, s44, s12
	v_readlane_b32 s45, v4, 5
	v_readlane_b32 s10, v4, 13
	v_readlane_b32 s11, v4, 21
	v_readlane_b32 s12, v4, 29
	s_add_i32 s45, s45, s10
	s_add_i32 s45, s45, s11
	s_add_i32 s45, s45, s12
	v_readlane_b32 s46, v4, 6
	v_readlane_b32 s10, v4, 14
	v_readlane_b32 s11, v4, 22
	v_readlane_b32 s12, v4, 30
	s_add_i32 s46, s46, s10
	s_add_i32 s46, s46, s11
	s_add_i32 s46, s46, s12
	v_readlane_b32 s47, v4, 7
	v_readlane_b32 s10, v4, 15
	v_readlane_b32 s11, v4, 23
	v_readlane_b32 s12, v4, 31
	s_add_i32 s47, s47, s10
	s_add_i32 s47, s47, s11
	s_add_i32 s47, s47, s12
	s_cmpk_eq_i32 s3, 0x100
	s_cselect_b32 s9, 1, 0
	s_cmp_gt_i32 s40, 12
	s_cselect_b32 s9, 0, s9
	s_cmp_gt_i32 s41, 12
	s_cselect_b32 s9, 0, s9
	s_cmp_gt_i32 s42, 12
	s_cselect_b32 s9, 0, s9
	s_cmp_gt_i32 s43, 12
	s_cselect_b32 s9, 0, s9
	s_cmp_gt_i32 s44, 12
	s_cselect_b32 s9, 0, s9
	s_cmp_gt_i32 s45, 12
	s_cselect_b32 s9, 0, s9
	s_cmp_gt_i32 s46, 12
	s_cselect_b32 s9, 0, s9
	s_cmp_gt_i32 s47, 12
	s_cselect_b32 s9, 0, s9
	s_cmp_eq_u32 s9, 0
	s_cbranch_scc1 .Lmoepro_slow
; __global__ void __launch_bounds__(512, 2) hymba_fwd(Args args) {
;     ...
;             int ok = (G == 256) ? 1 : 0, F = 0, rank = 0, mine = 0; const int x = bx & 7, j = bx >> 3;
;             for (int xx = 0; xx < 8; ++xx) { int tx = 0; for (int k = 0; k < 4; ++k) tx += tb[xx + 8 * k + 1] - tb[xx + 8 * k]; if (tx > 12) ok = 0;
;                 int f = 8 * tx - 64; f = f < 0 ? 0 : (f > 32 ? 32 : f);
;                 F += 32 - f; int below = j + (xx < x ? 1 : 0) - f; below = below < 0 ? 0 : (below > 32 - f ? 32 - f : below); rank += below; if (xx == x) mine = (j >= f) ? 1 : 0; }
;             tb[66] = ok; tb[67] = F; tb[68] = mine ? rank : -1;
;             for (int i = 0; i < MAXU; ++i) { int T = -1, e = 0, n = 0;
;                 if (ok) { const int U = i * 32 + j, LT = U >> 3; n = U & 7; int cum = 0;
;                     for (int k = 0; k < 4; ++k) { const int ee = x + 8 * k, t0 = tb[ee], nt = tb[ee + 1] - t0; if (T < 0 && LT < cum + nt) { e = ee; T = t0 + (LT - cum); } cum += nt; } }
;                 else { const int L = i * G + bx; if (L < acc * 8) { T = L >> 3; n = L & 7; for (int k = 1; k < 32; ++k) e += (tb[k] <= T) ? 1 : 0; } }
;                 tb[80 + 4 * i] = T; tb[81 + 4 * i] = e; tb[82 + 4 * i] = n; tb[83 + 4 * i] = T < 0 ? 0 : T - tb[e]; } }
	s_and_b32 s13, s2, 7
	s_lshr_b32 s14, s2, 3
	s_mov_b32 s48, 0
	s_mov_b32 s49, 0
	s_mov_b32 s50, 0
	s_lshl_b32 s15, s40, 3
	s_add_i32 s15, s15, -64
	s_max_i32 s15, s15, 0
	s_min_i32 s15, s15, 32
	s_sub_i32 s16, 32, s15
	s_add_i32 s48, s48, s16
	s_cmp_gt_u32 s13, 0
	s_cselect_b32 s17, 1, 0
	s_add_i32 s17, s17, s14
	s_sub_i32 s17, s17, s15
	s_max_i32 s17, s17, 0
	s_min_i32 s17, s17, s16
	s_add_i32 s49, s49, s17
	s_cmp_ge_i32 s14, s15
	s_cselect_b32 s18, 1, 0
	s_cmp_eq_u32 s13, 0
	s_cselect_b32 s50, s18, s50
	s_lshl_b32 s15, s41, 3
	s_add_i32 s15, s15, -64
	s_max_i32 s15, s15, 0
	s_min_i32 s15, s15, 32
	s_sub_i32 s16, 32, s15
	s_add_i32 s48, s48, s16
	s_cmp_gt_u32 s13, 1
	s_cselect_b32 s17, 1, 0
	s_add_i32 s17, s17, s14
	s_sub_i32 s17, s17, s15
	s_max_i32 s17, s17, 0
	s_min_i32 s17, s17, s16
	s_add_i32 s49, s49, s17
	s_cmp_ge_i32 s14, s15
	s_cselect_b32 s18, 1, 0
	s_cmp_eq_u32 s13, 1
	s_cselect_b32 s50, s18, s50
	s_lshl_b32 s15, s42, 3
	s_add_i32 s15, s15, -64
	s_max_i32 s15, s15, 0
	s_min_i32 s15, s15, 32
	s_sub_i32 s16, 32, s15
	s_add_i32 s48, s48, s16
	s_cmp_gt_u32 s13, 2
	s_cselect_b32 s17, 1, 0
	s_add_i32 s17, s17, s14
	s_sub_i32 s17, s17, s15
	s_max_i32 s17, s17, 0
	s_min_i32 s17, s17, s16
	s_add_i32 s49, s49, s17
	s_cmp_ge_i32 s14, s15
	s_cselect_b32 s18, 1, 0
	s_cmp_eq_u32 s13, 2
	s_cselect_b32 s50, s18, s50
	s_lshl_b32 s15, s43, 3
	s_add_i32 s15, s15, -64
	s_max_i32 s15, s15, 0
	s_min_i32 s15, s15, 32
	s_sub_i32 s16, 32, s15
	s_add_i32 s48, s48, s16
	s_cmp_gt_u32 s13, 3
	s_cselect_b32 s17, 1, 0
	s_add_i32 s17, s17, s14
	s_sub_i32 s17, s17, s15
	s_max_i32 s17, s17, 0
	s_min_i32 s17, s17, s16
	s_add_i32 s49, s49, s17
	s_cmp_ge_i32 s14, s15
	s_cselect_b32 s18, 1, 0
	s_cmp_eq_u32 s13, 3
	s_cselect_b32 s50, s18, s50
	s_lshl_b32 s15, s44, 3
	s_add_i32 s15, s15, -64
	s_max_i32 s15, s15, 0
	s_min_i32 s15, s15, 32
	s_sub_i32 s16, 32, s15
	s_add_i32 s48, s48, s16
	s_cmp_gt_u32 s13, 4
	s_cselect_b32 s17, 1, 0
	s_add_i32 s17, s17, s14
	s_sub_i32 s17, s17, s15
	s_max_i32 s17, s17, 0
	s_min_i32 s17, s17, s16
	s_add_i32 s49, s49, s17
	s_cmp_ge_i32 s14, s15
	s_cselect_b32 s18, 1, 0
	s_cmp_eq_u32 s13, 4
	s_cselect_b32 s50, s18, s50
	s_lshl_b32 s15, s45, 3
	s_add_i32 s15, s15, -64
	s_max_i32 s15, s15, 0
	s_min_i32 s15, s15, 32
	s_sub_i32 s16, 32, s15
	s_add_i32 s48, s48, s16
	s_cmp_gt_u32 s13, 5
	s_cselect_b32 s17, 1, 0
	s_add_i32 s17, s17, s14
	s_sub_i32 s17, s17, s15
	s_max_i32 s17, s17, 0
	s_min_i32 s17, s17, s16
	s_add_i32 s49, s49, s17
	s_cmp_ge_i32 s14, s15
	s_cselect_b32 s18, 1, 0
	s_cmp_eq_u32 s13, 5
	s_cselect_b32 s50, s18, s50
	s_lshl_b32 s15, s46, 3
	s_add_i32 s15, s15, -64
	s_max_i32 s15, s15, 0
	s_min_i32 s15, s15, 32
	s_sub_i32 s16, 32, s15
	s_add_i32 s48, s48, s16
	s_cmp_gt_u32 s13, 6
	s_cselect_b32 s17, 1, 0
	s_add_i32 s17, s17, s14
	s_sub_i32 s17, s17, s15
	s_max_i32 s17, s17, 0
	s_min_i32 s17, s17, s16
	s_add_i32 s49, s49, s17
	s_cmp_ge_i32 s14, s15
	s_cselect_b32 s18, 1, 0
	s_cmp_eq_u32 s13, 6
	s_cselect_b32 s50, s18, s50
	s_lshl_b32 s15, s47, 3
	s_add_i32 s15, s15, -64
	s_max_i32 s15, s15, 0
	s_min_i32 s15, s15, 32
	s_sub_i32 s16, 32, s15
	s_add_i32 s48, s48, s16
	s_cmp_gt_u32 s13, 7
	s_cselect_b32 s17, 1, 0
	s_add_i32 s17, s17, s14
	s_sub_i32 s17, s17, s15
	s_max_i32 s17, s17, 0
	s_min_i32 s17, s17, s16
	s_add_i32 s49, s49, s17
	s_cmp_ge_i32 s14, s15
	s_cselect_b32 s18, 1, 0
	s_cmp_eq_u32 s13, 7
	s_cselect_b32 s50, s18, s50
	s_cmp_lg_u32 s50, 0
	s_cselect_b32 s49, s49, -1
	v_mov_b32_e32 v6, 1
	v_mov_b32_e32 v7, s48
	v_mov_b32_e32 v8, s49
	s_add_i32 s15, 0, 0x22508
	v_mov_b32_e32 v9, s15
	ds_write2_b32 v9, v6, v7 offset1:1
	ds_write_b32 v9, v8 offset:8
	s_waitcnt lgkmcnt(0)
	s_add_i32 s6, 0, 0x22508
	v_mov_b32_e32 v1, s6
	ds_read_b32 v1, v1
	s_and_b32 s6, s2, 7
	s_lshr_b32 s7, s2, 3
	s_lshl_b32 s8, s6, 2
	s_add_i32 s8, s8, 0x22400
	v_mov_b32_e32 v2, s8
	ds_read2_b32 v[4:5], v2 offset1:1
	ds_read2_b32 v[6:7], v2 offset0:8 offset1:9
	ds_read2_b32 v[8:9], v2 offset0:16 offset1:17
	ds_read2_b32 v[10:11], v2 offset0:24 offset1:25
	ds_read_b32 v12, v2 offset:132
	ds_read_b32 v13, v2 offset:164
	ds_read_b32 v14, v2 offset:196
	ds_read_b32 v15, v2 offset:228
	s_waitcnt lgkmcnt(0)
	v_readfirstlane_b32 s9, v1
	v_readfirstlane_b32 s10, v4
	v_readfirstlane_b32 s14, v5
	v_readfirstlane_b32 s11, v6
	v_readfirstlane_b32 s15, v7
	v_readfirstlane_b32 s12, v8
	v_readfirstlane_b32 s16, v9
	v_readfirstlane_b32 s13, v10
	v_readfirstlane_b32 s17, v11
	v_readfirstlane_b32 s18, v12
	v_readfirstlane_b32 s19, v13
	v_readfirstlane_b32 s20, v14
	v_readfirstlane_b32 s21, v15
	s_cmp_eq_u32 s9, 0
	s_cbranch_scc1 .Lmo_done
	s_sub_i32 s14, s14, s10
	s_add_i32 s40, s14, -1
	s_lshl_b32 s44, s40, 8
	s_sub_i32 s18, s18, s44
	s_cmp_gt_i32 s14, 0
	s_cselect_b32 s18, s18, -1
	s_max_i32 s40, s40, 0
	s_sub_i32 s15, s15, s11
	s_add_i32 s41, s15, -1
	s_lshl_b32 s44, s41, 8
	s_sub_i32 s19, s19, s44
	s_cmp_gt_i32 s15, 0
	s_cselect_b32 s19, s19, -1
	s_max_i32 s41, s41, 0
	s_sub_i32 s16, s16, s12
	s_add_i32 s42, s16, -1
	s_lshl_b32 s44, s42, 8
	s_sub_i32 s20, s20, s44
	s_cmp_gt_i32 s16, 0
	s_cselect_b32 s20, s20, -1
	s_max_i32 s42, s42, 0
	s_sub_i32 s17, s17, s13
	s_add_i32 s43, s17, -1
	s_lshl_b32 s44, s43, 8
	s_sub_i32 s21, s21, s44
	s_cmp_gt_i32 s17, 0
	s_cselect_b32 s21, s21, -1
	s_max_i32 s43, s43, 0
	s_add_i32 s44, s40, s41
	s_add_i32 s44, s44, s42
	s_add_i32 s44, s44, s43
	s_mov_b32 s45, 0
	s_cmp_gt_i32 s14, 0
	s_addc_u32 s45, s45, 0
	s_cmp_gt_i32 s15, 0
	s_addc_u32 s45, s45, 0
	s_cmp_gt_i32 s16, 0
	s_addc_u32 s45, s45, 0
	s_cmp_gt_i32 s17, 0
	s_addc_u32 s45, s45, 0
	s_mov_b32 s46, 0
	s_cmp_gt_i32 s19, s18
	s_addc_u32 s46, s46, 0
	s_cmp_gt_i32 s20, s18
	s_addc_u32 s46, s46, 0
	s_cmp_gt_i32 s21, s18
	s_addc_u32 s46, s46, 0
	s_mov_b32 s47, 0
	s_cmp_ge_i32 s18, s19
	s_addc_u32 s47, s47, 0
	s_cmp_gt_i32 s20, s19
	s_addc_u32 s47, s47, 0
	s_cmp_gt_i32 s21, s19
	s_addc_u32 s47, s47, 0
	s_mov_b32 s48, 0
	s_cmp_ge_i32 s18, s20
	s_addc_u32 s48, s48, 0
	s_cmp_ge_i32 s19, s20
	s_addc_u32 s48, s48, 0
	s_cmp_gt_i32 s21, s20
	s_addc_u32 s48, s48, 0
	s_mov_b32 s49, 0
	s_cmp_ge_i32 s18, s21
	s_addc_u32 s49, s49, 0
	s_cmp_ge_i32 s19, s21
	s_addc_u32 s49, s49, 0
	s_cmp_ge_i32 s20, s21
	s_addc_u32 s49, s49, 0
	s_mov_b32 s50, 0

; __global__ void __launch_bounds__(512, 2) hymba_fwd(Args args) {
;     ...
;         if (tid == 0) { int acc = 0; for (int e = 0; e < NEXP; ++e) { const int c = tb[33 + e]; tb[e] = acc; acc += (c + 255) >> 8; } tb[32] = acc;
;             int ok = (G == 256) ? 1 : 0, F = 0, rank = 0, mine = 0; const int x = bx & 7, j = bx >> 3;
;             for (int xx = 0; xx < 8; ++xx) { int tx = 0; for (int k = 0; k < 4; ++k) tx += tb[xx + 8 * k + 1] - tb[xx + 8 * k]; if (tx > 12) ok = 0;
;                 int f = 8 * tx - 64; f = f < 0 ? 0 : (f > 32 ? 32 : f);
.Lmo_done:
	s_waitcnt lgkmcnt(0)
	s_branch .Lmoepro_done
.Lmoepro_slow:
	v_cmp_eq_u32_e32 vcc, 0, v28
	s_nop 1
	s_and_saveexec_b64 s[6:7], vcc
	s_cbranch_execz .LBB0_701
	s_add_i32 s0, 0, 0x22484
	v_mov_b32_e32 v0, s0
	ds_read2_b32 v[0:1], v0 offset1:1
	s_add_i32 s0, 0, 0x2248c
	v_mov_b32_e32 v2, s0
	s_add_i32 s0, 0, 0x22494
	v_mov_b32_e32 v4, s0
	s_add_i32 s0, 0, 0x2249c
	v_mov_b32_e32 v5, s0
	ds_read2_b32 v[2:3], v2 offset1:1
	ds_read2_b32 v[8:9], v4 offset1:1
	ds_read2_b32 v[10:11], v5 offset1:1
	s_waitcnt lgkmcnt(3)
	v_add_u32_e32 v0, 0xff, v0
	v_ashrrev_i32_e32 v5, 8, v0
	v_add_u32_e32 v0, 0xff, v1
	v_ashrrev_i32_e32 v0, 8, v0
	v_add_u32_e32 v6, v0, v5
	s_waitcnt lgkmcnt(2)
	v_add_u32_e32 v0, 0xff, v2
	v_ashrrev_i32_e32 v0, 8, v0
	s_add_i32 s12, 0, 0x22400
	v_add_u32_e32 v7, v0, v6
	v_mov_b32_e32 v4, 0
	v_mov_b32_e32 v0, s12
	ds_write_b128 v0, v[4:7]
	v_add_u32_e32 v0, 0xff, v3
	v_ashrrev_i32_e32 v0, 8, v0
	s_waitcnt lgkmcnt(2)
	v_add_u32_e32 v1, 0xff, v8
	v_add_u32_e32 v0, v0, v7
	v_ashrrev_i32_e32 v1, 8, v1
	v_add_u32_e32 v2, 0xff, v9
	v_add_u32_e32 v1, v1, v0
	v_ashrrev_i32_e32 v2, 8, v2
	s_waitcnt lgkmcnt(1)
	v_add_u32_e32 v3, 0xff, v10
	v_add_u32_e32 v2, v2, v1
	v_ashrrev_i32_e32 v3, 8, v3
	s_add_i32 s0, 0, 0x22410
	v_add_u32_e32 v3, v3, v2
	v_mov_b32_e32 v8, s0
	ds_write_b128 v8, v[0:3]
	v_add_u32_e32 v8, 0xff, v11
	v_ashrrev_i32_e32 v8, 8, v8
	s_add_i32 s0, 0, 0x224a4
	v_add_u32_e32 v24, v8, v3
	v_mov_b32_e32 v8, s0
	ds_read2_b32 v[8:9], v8 offset1:1
	s_add_i32 s0, 0, 0x224ac
	v_mov_b32_e32 v10, s0
	s_add_i32 s0, 0, 0x224b4
	v_mov_b32_e32 v12, s0
	s_add_i32 s0, 0, 0x224c4
	v_mov_b32_e32 v14, s0
	s_waitcnt lgkmcnt(0)
	v_add_u32_e32 v8, 0xff, v8
	ds_read2_b32 v[10:11], v10 offset1:1
	ds_read2_b32 v[12:13], v12 offset1:1
	ds_read2_b32 v[14:15], v14 offset1:1
	v_ashrrev_i32_e32 v8, 8, v8
	v_add_u32_e32 v25, v8, v24
	v_add_u32_e32 v8, 0xff, v9
	v_ashrrev_i32_e32 v8, 8, v8
	v_add_u32_e32 v26, v8, v25
	s_waitcnt lgkmcnt(2)
	v_add_u32_e32 v8, 0xff, v10
	s_add_i32 s0, 0, 0x22420
	v_ashrrev_i32_e32 v8, 8, v8
	v_mov_b32_e32 v20, s0
	s_add_i32 s0, 0, 0x224bc
	v_add_u32_e32 v27, v8, v26
	v_add_u32_e32 v8, 0xff, v11
	v_mov_b32_e32 v11, s0
	s_waitcnt lgkmcnt(1)
	v_add_u32_e32 v9, 0xff, v12
	v_add_u32_e32 v10, 0xff, v13
	ds_read2_b32 v[12:13], v11 offset1:1
	s_add_i32 s0, 0, 0x224cc
	v_ashrrev_i32_e32 v8, 8, v8
	v_mov_b32_e32 v11, s0
	s_add_i32 s0, 0, 0x224d4
	ds_write_b128 v20, v[24:27]
	v_add_u32_e32 v8, v8, v27
	v_ashrrev_i32_e32 v9, 8, v9
	v_mov_b32_e32 v18, s0
	v_add_u32_e32 v9, v9, v8
	v_ashrrev_i32_e32 v10, 8, v10
	ds_read2_b32 v[16:17], v11 offset1:1
	ds_read2_b32 v[18:19], v18 offset1:1
	ds_read_b32 v24, v20
	s_waitcnt lgkmcnt(4)
	v_add_u32_e32 v11, 0xff, v12
	v_add_u32_e32 v10, v10, v9
	v_ashrrev_i32_e32 v11, 8, v11
	s_add_i32 s0, 0, 0x22430
	v_add_u32_e32 v11, v11, v10
	v_mov_b32_e32 v12, s0
	ds_write_b128 v12, v[8:11]
	v_add_u32_e32 v12, 0xff, v13
	v_ashrrev_i32_e32 v20, 8, v12
	v_add_u32_e32 v12, 0xff, v14
	v_ashrrev_i32_e32 v21, 8, v12
	v_add_u32_e32 v12, 0xff, v15
	v_ashrrev_i32_e32 v22, 8, v12
	s_waitcnt lgkmcnt(3)
	v_add_u32_e32 v12, 0xff, v16
	v_ashrrev_i32_e32 v23, 8, v12
	v_add_u32_e32 v12, 0xff, v17
	v_ashrrev_i32_e32 v29, 8, v12
	s_waitcnt lgkmcnt(2)
	v_add_u32_e32 v12, 0xff, v18
	v_ashrrev_i32_e32 v30, 8, v12
	v_add_u32_e32 v12, 0xff, v19
	s_add_i32 s0, 0, 0x224dc
	v_ashrrev_i32_e32 v31, 8, v12
	v_mov_b32_e32 v12, s0
	s_add_i32 s0, 0, 0x224e4
	ds_read2_b32 v[12:13], v12 offset1:1
	v_mov_b32_e32 v14, s0
	s_add_i32 s0, 0, 0x224ec
	v_mov_b32_e32 v16, s0
	s_add_i32 s0, 0, 0x224f4
	v_mov_b32_e32 v18, s0
	ds_read2_b32 v[14:15], v14 offset1:1
	ds_read2_b32 v[16:17], v16 offset1:1
	ds_read2_b32 v[18:19], v18 offset1:1
	s_waitcnt lgkmcnt(3)
	v_add_u32_e32 v12, 0xff, v12
	v_ashrrev_i32_e32 v32, 8, v12
	v_add_u32_e32 v12, 0xff, v13
	s_waitcnt lgkmcnt(2)
	v_add_u32_e32 v13, 0xff, v15
	v_ashrrev_i32_e32 v34, 8, v13
	s_waitcnt lgkmcnt(1)
	v_add_u32_e32 v13, 0xff, v16
	v_ashrrev_i32_e32 v35, 8, v13
	v_add_u32_e32 v13, 0xff, v17
	v_ashrrev_i32_e32 v38, 8, v13
	s_waitcnt lgkmcnt(0)
	v_add_u32_e32 v13, 0xff, v18
	s_add_i32 s0, 0, 0x224fc
	v_ashrrev_i32_e32 v39, 8, v13
	v_add_u32_e32 v13, 0xff, v19
	s_cmpk_eq_i32 s3, 0x100
	v_ashrrev_i32_e32 v40, 8, v13
	v_mov_b32_e32 v13, s0
	s_cselect_b64 s[0:1], -1, 0
	s_and_b32 s13, s2, 7
	s_ashr_i32 s14, s2, 3
	s_cmp_lg_u32 s13, 0
	s_cselect_b64 s[8:9], -1, 0
	s_cmp_lg_u64 s[8:9], 0
	s_addc_u32 s18, s14, 0
	s_cmp_eq_u32 s13, 0
	s_cselect_b64 s[8:9], -1, 0
	s_cmp_gt_u32 s13, 1
	s_cselect_b64 s[10:11], -1, 0
	s_cmp_lg_u64 s[10:11], 0
	s_addc_u32 s17, s14, 0
	s_cmp_gt_u32 s13, 2
	s_cselect_b64 s[10:11], -1, 0
	s_cmp_lg_u64 s[10:11], 0
	s_addc_u32 s16, s14, 0
	s_cmp_gt_u32 s13, 3
	s_cselect_b64 s[10:11], -1, 0
	s_cmp_lg_u64 s[10:11], 0
	s_addc_u32 s15, s14, 0
	s_cmp_gt_u32 s13, 4
	s_cselect_b64 s[10:11], -1, 0
	s_cmp_lg_u64 s[10:11], 0
	s_addc_u32 s11, s14, 0
	s_cmp_gt_u32 s13, 5
	s_cselect_b64 s[20:21], -1, 0
	s_cmp_lg_u64 s[20:21], 0
	v_add_u32_e32 v20, v20, v11
	s_addc_u32 s10, s14, 0
	s_add_i32 s19, 0, 0x22428
	v_add_u32_e32 v21, v21, v20
	v_ashrrev_i32_e32 v33, 8, v12
	v_add_u32_e32 v12, 0xff, v14
	v_mov_b32_e32 v36, s19
	v_add_u32_e32 v22, v22, v21
	s_add_i32 s19, 0, 0x22440
	v_ashrrev_i32_e32 v17, 8, v12
	v_add_u32_e32 v23, v23, v22
	v_mov_b32_e32 v12, s19
	ds_write_b128 v12, v[20:23]
	v_add_u32_e32 v12, v29, v23
	ds_read2_b32 v[26:27], v13 offset1:1
	v_add_u32_e32 v13, v30, v12
	v_add_u32_e32 v14, v31, v13
	v_add_u32_e32 v15, v32, v14
	v_add_u32_e32 v16, v33, v15
	s_add_i32 s19, 0, 0x22448
	v_add_u32_e32 v17, v17, v16
	v_mov_b32_e32 v29, s19
	v_add_u32_e32 v18, v34, v17
	s_add_i32 s19, 0, 0x22460
	v_add_u32_e32 v19, v35, v18
	v_mov_b32_e32 v22, s19
	s_add_i32 s19, 0, 0x22468
	ds_write_b128 v22, v[16:19]
	v_mov_b32_e32 v30, s19
	ds_read_b64 v[22:23], v36
	ds_read_b64 v[34:35], v29
	ds_read_b64 v[36:37], v30
	v_add_u32_e32 v30, v38, v19
	s_waitcnt lgkmcnt(4)
; __global__ void __launch_bounds__(512, 2) hymba_fwd(Args args) {
;     ...
;         if (tid == 0) { int acc = 0; for (int e = 0; e < NEXP; ++e) { const int c = tb[33 + e]; tb[e] = acc; acc += (c + 255) >> 8; } tb[32] = acc;
;             int ok = (G == 256) ? 1 : 0, F = 0, rank = 0, mine = 0; const int x = bx & 7, j = bx >> 3;
;             for (int xx = 0; xx < 8; ++xx) { int tx = 0; for (int k = 0; k < 4; ++k) tx += tb[xx + 8 * k + 1] - tb[xx + 8 * k]; if (tx > 12) ok = 0;
;                 int f = 8 * tx - 64; f = f < 0 ? 0 : (f > 32 ? 32 : f);
;                 F += 32 - f; int below = j + (xx < x ? 1 : 0) - f; below = below < 0 ? 0 : (below > 32 - f ? 32 - f : below); rank += below; if (xx == x) mine = (j >= f) ? 1 : 0; }
;             tb[66] = ok; tb[67] = F; tb[68] = mine ? rank : -1;
	v_add_u32_e32 v26, 0xff, v26
	v_add_u32_e32 v31, v39, v30
	v_ashrrev_i32_e32 v26, 8, v26
	v_add_u32_e32 v27, 0xff, v27
	v_add_u32_e32 v0, v0, v8
	v_add_u32_e32 v32, v40, v31
	s_add_i32 s19, 0, 0x22470
	v_ashrrev_i32_e32 v27, 8, v27
	v_add_u32_e32 v2, v2, v10
	v_add_u32_e32 v10, v0, v12
	v_add_u32_e32 v33, v26, v32
	v_mov_b32_e32 v0, s19
	s_add_i32 s19, 0, 0x22480
	v_add_u32_e32 v5, v5, v25
	ds_write_b128 v0, v[30:33]
	v_add_u32_e32 v25, v27, v33
	v_mov_b32_e32 v0, s19
	ds_write_b32 v0, v25
	s_waitcnt lgkmcnt(4)
	v_add_u32_e32 v0, v6, v22
	v_add_u32_e32 v5, v5, v21
	s_waitcnt lgkmcnt(3)
	v_add_u32_e32 v21, v0, v34
	v_add_u32_e32 v0, v7, v23
	s_add_i32 s19, 0, 0x22474
	v_add_u32_e32 v1, v1, v9
	v_add_u32_e32 v22, v0, v35
	v_add_u32_e32 v0, v24, v20
	v_mov_b32_e32 v6, s19
	v_add_u32_e32 v9, v1, v13
	v_add_u32_e32 v23, v0, v16
	ds_read2_b32 v[0:1], v6 offset1:1
	ds_read2_b32 v[6:7], v6 offset0:2 offset1:3
	v_add_u32_e32 v8, v3, v11
	v_add_u32_e32 v8, v8, v15
	v_add_u32_e32 v2, v2, v14
	v_add_u32_e32 v5, v5, v17
	v_add_u32_e32 v17, v18, v21
	v_add_u32_e32 v10, v10, v30
	s_waitcnt lgkmcnt(1)
	v_add_u32_e32 v0, v9, v0
	v_add_u32_e32 v1, v2, v1
	s_waitcnt lgkmcnt(0)
	v_add_u32_e32 v2, v8, v6
	v_add_u32_e32 v6, v23, v7
	v_add_u32_e32 v8, v22, v37
	v_sub_u32_e32 v9, v17, v5
	v_sub_u32_e32 v5, v5, v23
	v_sub_u32_e32 v6, v6, v2
	v_sub_u32_e32 v2, v2, v1
	v_sub_u32_e32 v1, v1, v0
	v_sub_u32_e32 v0, v0, v10
	v_sub_u32_e32 v8, v10, v8
	v_lshlrev_b32_e32 v10, 3, v5
	v_mov_b32_e32 v17, 0x60
	v_med3_i32 v10, v10, 64, v17
	v_subrev_u32_e32 v18, 64, v10
	v_cmp_ge_i32_e32 vcc, s14, v18
	v_lshlrev_b32_e32 v18, 3, v9
	v_add_u32_e32 v19, v19, v22
	v_add_u32_e32 v7, v21, v36
	v_med3_i32 v18, v18, 64, v17
	v_sub_u32_e32 v7, v19, v7
	s_and_b64 s[8:9], s[8:9], vcc
	v_subrev_u32_e32 v19, 64, v18
	s_cmp_eq_u32 s13, 1
	v_cmp_ge_i32_e32 vcc, s14, v19
	v_cndmask_b32_e64 v21, 0, 1, s[8:9]
	s_nop 0
	v_cndmask_b32_e64 v19, 0, 1, vcc
	s_cselect_b64 vcc, -1, 0
	v_cndmask_b32_e32 v19, v21, v19, vcc
	v_lshlrev_b32_e32 v21, 3, v7
	v_med3_i32 v21, v21, 64, v17
	v_subrev_u32_e32 v22, 64, v21
	s_cmp_eq_u32 s13, 2
	v_cmp_ge_i32_e32 vcc, s14, v22
	s_nop 1
	v_cndmask_b32_e64 v22, 0, 1, vcc
	s_cselect_b64 vcc, -1, 0
	v_cndmask_b32_e32 v19, v19, v22, vcc
	v_lshlrev_b32_e32 v22, 3, v8
	v_med3_i32 v22, v22, 64, v17
	v_subrev_u32_e32 v23, 64, v22
	s_cmp_eq_u32 s13, 3
	v_cmp_ge_i32_e32 vcc, s14, v23
	s_nop 1
	v_cndmask_b32_e64 v23, 0, 1, vcc
	s_cselect_b64 vcc, -1, 0
	v_cndmask_b32_e32 v19, v19, v23, vcc
	v_lshlrev_b32_e32 v23, 3, v0
	v_med3_i32 v23, v23, 64, v17
	v_subrev_u32_e32 v26, 64, v23
	s_cmp_eq_u32 s13, 4
	v_cmp_ge_i32_e32 vcc, s14, v26
	s_nop 1
	v_cndmask_b32_e64 v26, 0, 1, vcc
	s_cselect_b64 vcc, -1, 0
	v_cndmask_b32_e32 v19, v19, v26, vcc
	v_lshlrev_b32_e32 v26, 3, v1
	v_med3_i32 v26, v26, 64, v17
	v_subrev_u32_e32 v27, 64, v26
	s_cmp_eq_u32 s13, 5
	v_cmp_ge_i32_e32 vcc, s14, v27
	s_nop 1
	v_cndmask_b32_e64 v27, 0, 1, vcc
	s_cselect_b64 vcc, -1, 0
	v_cndmask_b32_e32 v19, v19, v27, vcc
	v_lshlrev_b32_e32 v27, 3, v2
	v_med3_i32 v27, v27, 64, v17
	v_subrev_u32_e32 v29, 64, v27
	s_cmp_eq_u32 s13, 6
	v_cmp_ge_i32_e32 vcc, s14, v29
	s_nop 1
	v_cndmask_b32_e64 v29, 0, 1, vcc
	s_cselect_b64 vcc, -1, 0
	v_cndmask_b32_e32 v19, v19, v29, vcc
	v_lshlrev_b32_e32 v29, 3, v6
	v_med3_i32 v17, v29, 64, v17
	v_subrev_u32_e32 v29, 64, v17
	s_cmp_eq_u32 s13, 7
	v_cmp_ge_i32_e32 vcc, s14, v29
	s_nop 1
	v_cndmask_b32_e64 v29, 0, 1, vcc
	s_cselect_b64 vcc, -1, 0
	s_cmp_lg_u64 vcc, 0
	s_addc_u32 s8, s14, 0
	s_add_i32 s9, 0, 0x22450
	v_cndmask_b32_e32 v19, v19, v29, vcc
	v_mov_b32_e32 v29, s9
	ds_write_b128 v29, v[12:15]
	v_sub_u32_e32 v12, 0x60, v10
	v_sub_u32_e32 v10, s18, v10
	v_add_u32_e32 v13, 64, v10
	s_movk_i32 s18, 0xffbf
	v_min_i32_e32 v13, v13, v12
	v_cmp_lt_i32_e32 vcc, s18, v10
	s_nop 1
	v_cndmask_b32_e32 v10, 0, v13, vcc
	v_sub_u32_e32 v13, 0x60, v18
	v_sub_u32_e32 v18, s17, v18
	v_add_u32_e32 v29, 64, v18
	v_add_u32_e32 v12, v13, v12
	v_min_i32_e32 v13, v29, v13
	v_cmp_lt_i32_e32 vcc, s18, v18
	v_sub_u32_e32 v18, s16, v21
	s_nop 0
	v_cndmask_b32_e32 v13, 0, v13, vcc
	v_add_u32_e32 v10, v13, v10
	v_sub_u32_e32 v13, 0x60, v21
	v_add_u32_e32 v21, 64, v18
	v_add_u32_e32 v12, v13, v12
	v_min_i32_e32 v13, v21, v13
	v_cmp_lt_i32_e32 vcc, s18, v18
	v_sub_u32_e32 v18, s15, v22
	v_add_u32_e32 v21, 64, v18
	v_cndmask_b32_e32 v13, 0, v13, vcc
	v_add_u32_e32 v10, v13, v10
	v_sub_u32_e32 v13, 0x60, v22
	v_add_u32_e32 v12, v13, v12
	v_min_i32_e32 v13, v21, v13
	v_cmp_lt_i32_e32 vcc, s18, v18
	v_sub_u32_e32 v18, s11, v23
	v_add_u32_e32 v21, 64, v18
	v_cndmask_b32_e32 v13, 0, v13, vcc
	v_add_u32_e32 v10, v13, v10
	v_sub_u32_e32 v13, 0x60, v23
	v_add_u32_e32 v12, v13, v12
	v_min_i32_e32 v13, v21, v13
	v_cmp_lt_i32_e32 vcc, s18, v18
	v_sub_u32_e32 v18, s10, v26
	v_add_u32_e32 v21, 64, v18
	v_cndmask_b32_e32 v13, 0, v13, vcc
	v_add_u32_e32 v10, v13, v10
	v_sub_u32_e32 v13, 0x60, v26
	v_add_u32_e32 v12, v13, v12
	v_min_i32_e32 v13, v21, v13
	v_cmp_lt_i32_e32 vcc, s18, v18
	v_sub_u32_e32 v18, s8, v27
	v_add_u32_e32 v21, 64, v18
	v_cndmask_b32_e32 v13, 0, v13, vcc
	v_add_u32_e32 v10, v13, v10
	v_sub_u32_e32 v13, 0x60, v27
	v_add_u32_e32 v12, v13, v12
	v_min_i32_e32 v13, v21, v13
	v_cmp_lt_i32_e32 vcc, s18, v18
	s_nop 1
	v_cndmask_b32_e32 v13, 0, v13, vcc
	v_cmp_lt_i32_e32 vcc, 12, v0
	v_add_u32_e32 v10, v13, v10
	s_nop 0
	v_cndmask_b32_e64 v0, 0, 1, vcc
	v_cmp_lt_i32_e32 vcc, 12, v1
	v_readfirstlane_b32 s8, v0
	s_lshl_b32 s8, s8, 3
	v_cndmask_b32_e64 v0, 0, 1, vcc
; __global__ void __launch_bounds__(512, 2) hymba_fwd(Args args) {
;     ...
;             for (int xx = 0; xx < 8; ++xx) { int tx = 0; for (int k = 0; k < 4; ++k) tx += tb[xx + 8 * k + 1] - tb[xx + 8 * k]; if (tx > 12) ok = 0;
;                 int f = 8 * tx - 64; f = f < 0 ? 0 : (f > 32 ? 32 : f);
;                 F += 32 - f; int below = j + (xx < x ? 1 : 0) - f; below = below < 0 ? 0 : (below > 32 - f ? 32 - f : below); rank += below; if (xx == x) mine = (j >= f) ? 1 : 0; }
;             tb[66] = ok; tb[67] = F; tb[68] = mine ? rank : -1;
;             for (int i = 0; i < MAXU; ++i) { int T = -1, e = 0, n = 0;
;                 if (ok) { const int U = i * 32 + j, LT = U >> 3; n = U & 7; int cum = 0;
;                     for (int k = 0; k < 4; ++k) { const int ee = x + 8 * k, t0 = tb[ee], nt = tb[ee + 1] - t0; if (T < 0 && LT < cum + nt) { e = ee; T = t0 + (LT - cum); } cum += nt; } }
;                 else { const int L = i * G + bx; if (L < acc * 8) { T = L >> 3; n = L & 7; for (int k = 1; k < 32; ++k) e += (tb[k] <= T) ? 1 : 0; } }
;                 tb[80 + 4 * i] = T; tb[81 + 4 * i] = e; tb[82 + 4 * i] = n; tb[83 + 4 * i] = T < 0 ? 0 : T - tb[e]; } }
	v_cmp_lt_i32_e32 vcc, 12, v2
	v_readfirstlane_b32 s9, v0
	s_lshl_b32 s9, s9, 2
	v_cndmask_b32_e64 v0, 0, 1, vcc
	v_cmp_lt_i32_e32 vcc, 12, v6
	s_or_b32 s8, s8, s9
	v_readfirstlane_b32 s9, v0
	v_cndmask_b32_e64 v0, 0, 1, vcc
	s_lshl_b32 s9, s9, 1
	v_readfirstlane_b32 s10, v0
	s_or_b32 s9, s10, s9
	v_cmp_lt_i32_e32 vcc, 12, v5
	s_and_b32 s9, s9, 3
	s_or_b32 s8, s9, s8
	v_cndmask_b32_e64 v0, 0, 1, vcc
	v_cmp_lt_i32_e32 vcc, 12, v9
	v_readfirstlane_b32 s9, v0
	s_lshl_b32 s9, s9, 3
	v_cndmask_b32_e64 v0, 0, 1, vcc
	v_cmp_lt_i32_e32 vcc, 12, v7
	v_readfirstlane_b32 s10, v0
	s_lshl_b32 s10, s10, 2
	v_cndmask_b32_e64 v0, 0, 1, vcc
	v_cmp_lt_i32_e32 vcc, 12, v8
	s_or_b32 s9, s9, s10
	v_readfirstlane_b32 s10, v0
	v_cndmask_b32_e64 v0, 0, 1, vcc
	s_lshl_b32 s10, s10, 1
	v_readfirstlane_b32 s11, v0
	s_or_b32 s10, s11, s10
	s_and_b32 s10, s10, 3
	s_or_b32 s9, s10, s9
	s_and_b32 s8, s8, 15
	s_lshl_b32 s9, s9, 4
	s_or_b32 s8, s8, s9
	s_and_b32 s8, s8, 0xff
	s_cmp_eq_u32 s8, 0
	v_sub_u32_e32 v5, s14, v17
	s_cselect_b64 s[8:9], -1, 0
	v_sub_u32_e32 v2, 0x60, v17
	v_add_u32_e32 v6, 64, v5
	s_and_b64 s[0:1], s[8:9], s[0:1]
	v_add_u32_e32 v1, v2, v12
	v_min_i32_e32 v2, v6, v2
	v_cmp_lt_i32_e32 vcc, s18, v5
	v_cndmask_b32_e64 v0, 0, 1, s[0:1]
	s_xor_b64 s[8:9], s[0:1], -1
	v_cndmask_b32_e32 v2, 0, v2, vcc
	v_and_b32_e32 v5, 1, v19
	s_add_i32 s0, 0, 0x22508
	v_add_u32_e32 v2, v2, v10
	v_mov_b32_e32 v6, s0
	v_cmp_eq_u32_e32 vcc, 1, v5
	s_add_i32 s0, 0, 0x22510
	s_mov_b64 s[10:11], -1
	ds_write_b64 v6, v[0:1]
	s_mov_b32 s1, -1
	v_cndmask_b32_e32 v0, -1, v2, vcc
	v_mov_b32_e32 v1, s0
	v_lshlrev_b32_e32 v5, 3, v25
	s_and_b64 vcc, exec, s[8:9]
	ds_write_b32 v1, v0
	s_cbranch_vccz .LBB0_682
	v_cmp_ge_i32_e32 vcc, s2, v5
	s_mov_b32 s0, 0
	s_cbranch_vccnz .LBB0_681
	s_add_i32 s0, 0, 0x22404
	v_mov_b32_e32 v0, s0
	ds_read2_b32 v[0:1], v0 offset1:1
	s_add_i32 s0, 0, 0x2240c
	v_mov_b32_e32 v2, s0
	s_add_i32 s0, 0, 0x22414
	v_mov_b32_e32 v4, s0
	s_add_i32 s0, 0, 0x22424
	v_mov_b32_e32 v10, s0
	ds_read2_b32 v[6:7], v2 offset1:1
	ds_read2_b32 v[8:9], v4 offset1:1
	ds_read2_b32 v[12:13], v10 offset1:1
	s_waitcnt lgkmcnt(3)
	v_cmp_ge_i32_e32 vcc, s14, v0
	s_add_i32 s0, 0, 0x2242c
	s_mov_b32 s1, s14
	v_cndmask_b32_e64 v0, 0, 1, vcc
	v_cmp_ge_i32_e32 vcc, s14, v1
	s_nop 1
	v_cndmask_b32_e64 v1, 0, 1, vcc
	s_waitcnt lgkmcnt(2)
	v_cmp_ge_i32_e32 vcc, s14, v6
	s_nop 1
	v_addc_co_u32_e32 v0, vcc, v0, v1, vcc
	v_cmp_ge_i32_e32 vcc, s14, v7
	s_nop 1
	v_cndmask_b32_e64 v1, 0, 1, vcc
	s_waitcnt lgkmcnt(1)
	v_cmp_ge_i32_e32 vcc, s14, v8
	s_nop 1
	v_addc_co_u32_e32 v0, vcc, v0, v1, vcc
	v_cmp_ge_i32_e32 vcc, s14, v9
	s_nop 1
	v_cndmask_b32_e64 v1, 0, 1, vcc
	v_cmp_ge_i32_e32 vcc, s14, v3
	s_nop 1
	v_addc_co_u32_e32 v0, vcc, v0, v1, vcc
	v_cmp_ge_i32_e32 vcc, s14, v24
	s_nop 1
	v_cndmask_b32_e64 v1, 0, 1, vcc
	s_waitcnt lgkmcnt(0)
	v_cmp_ge_i32_e32 vcc, s14, v12
	s_nop 1
	v_addc_co_u32_e32 v4, vcc, v0, v1, vcc
	v_mov_b32_e32 v0, s0
	ds_read2_b32 v[0:1], v0 offset1:1
	s_add_i32 s0, 0, 0x22434
	v_mov_b32_e32 v2, s0
	s_add_i32 s0, 0, 0x22444
	v_mov_b32_e32 v6, s0
	s_add_i32 s0, 0, 0x2244c
	v_cmp_ge_i32_e32 vcc, s14, v13
	v_mov_b32_e32 v8, s0
	ds_read2_b32 v[2:3], v2 offset1:1
	ds_read2_b32 v[6:7], v6 offset1:1
	ds_read2_b32 v[8:9], v8 offset1:1
	v_cndmask_b32_e64 v10, 0, 1, vcc
	s_waitcnt lgkmcnt(3)
	v_cmp_ge_i32_e32 vcc, s14, v0
	s_add_i32 s0, 0, 0x22454
	s_nop 0
	v_addc_co_u32_e32 v0, vcc, v4, v10, vcc
	v_cmp_ge_i32_e32 vcc, s14, v1
	s_nop 1
	v_cndmask_b32_e64 v1, 0, 1, vcc
	s_waitcnt lgkmcnt(2)
	v_cmp_ge_i32_e32 vcc, s14, v2
	s_nop 1
	v_addc_co_u32_e32 v0, vcc, v0, v1, vcc
	v_cmp_ge_i32_e32 vcc, s14, v3
	s_nop 1
	v_cndmask_b32_e64 v1, 0, 1, vcc
	v_cmp_ge_i32_e32 vcc, s14, v11
	s_nop 1
	v_addc_co_u32_e32 v0, vcc, v0, v1, vcc
	v_cmp_ge_i32_e32 vcc, s14, v20
	s_nop 1
	v_cndmask_b32_e64 v1, 0, 1, vcc
	s_waitcnt lgkmcnt(1)
	v_cmp_ge_i32_e32 vcc, s14, v6
	s_nop 1
	v_addc_co_u32_e32 v0, vcc, v0, v1, vcc
	v_cmp_ge_i32_e32 vcc, s14, v7
	s_nop 1
	v_cndmask_b32_e64 v1, 0, 1, vcc
	s_waitcnt lgkmcnt(0)
	v_cmp_ge_i32_e32 vcc, s14, v8
	s_nop 1
	v_addc_co_u32_e32 v4, vcc, v0, v1, vcc
	v_mov_b32_e32 v0, s0
	v_cmp_ge_i32_e32 vcc, s14, v9
	ds_read_b32 v9, v0
	s_add_i32 s0, 0, 0x22464
	v_cndmask_b32_e64 v8, 0, 1, vcc
	v_mov_b32_e32 v0, s0
	s_add_i32 s0, 0, 0x2246c
	s_waitcnt lgkmcnt(0)
	v_cmp_ge_i32_e32 vcc, s14, v9
	v_mov_b32_e32 v2, s0
	s_add_i32 s0, 0, 0x22474
	v_addc_co_u32_e32 v4, vcc, v4, v8, vcc
	v_mov_b32_e32 v6, s0
	v_cmp_ge_i32_e32 vcc, s14, v14
	ds_read2_b32 v[0:1], v0 offset1:1
	ds_read2_b32 v[2:3], v2 offset1:1
	ds_read2_b32 v[6:7], v6 offset1:1
	v_cndmask_b32_e64 v8, 0, 1, vcc
	v_cmp_ge_i32_e32 vcc, s14, v15
	s_add_i32 s0, 0, 0x2247c
	s_nop 0
	v_addc_co_u32_e32 v4, vcc, v4, v8, vcc
	v_cmp_ge_i32_e32 vcc, s14, v16
	s_nop 1
	v_cndmask_b32_e64 v8, 0, 1, vcc
	s_waitcnt lgkmcnt(2)
	v_cmp_ge_i32_e32 vcc, s14, v0
	s_nop 1
	v_addc_co_u32_e32 v0, vcc, v4, v8, vcc
	v_cmp_ge_i32_e32 vcc, s14, v1
	s_nop 1
	v_cndmask_b32_e64 v1, 0, 1, vcc
	s_waitcnt lgkmcnt(1)
	v_cmp_ge_i32_e32 vcc, s14, v2
	v_mov_b32_e32 v2, s0
	ds_read_b32 v2, v2
	v_addc_co_u32_e32 v0, vcc, v0, v1, vcc
	v_cmp_ge_i32_e32 vcc, s14, v3
	s_mov_b32 s0, s13
	s_nop 0
	v_cndmask_b32_e64 v1, 0, 1, vcc
	s_waitcnt lgkmcnt(1)
	v_cmp_ge_i32_e32 vcc, s14, v6
	s_nop 1
	v_addc_co_u32_e32 v0, vcc, v0, v1, vcc
	v_cmp_ge_i32_e32 vcc, s14, v7
	s_nop 1
	v_cndmask_b32_e64 v1, 0, 1, vcc
	s_waitcnt lgkmcnt(0)
	v_cmp_ge_i32_e32 vcc, s14, v2
	s_nop 1
	v_addc_co_u32_e32 v4, vcc, v0, v1, vcc

;     __device__ __forceinline__ bool next(int i, Unit& u) const {
;         if (i >= MAXU) return false;
;         const int T = __builtin_amdgcn_readfirstlane(tb[80 + 4 * i]); if (T < 0) return false;
;         const int e = __builtin_amdgcn_readfirstlane(tb[81 + 4 * i]), n = __builtin_amdgcn_readfirstlane(tb[82 + 4 * i]);
;         u.pm = T; u.pn = e * 8 + n; u.e = e; u.lt = __builtin_amdgcn_readfirstlane(tb[83 + 4 * i]); u.slot = i; return true;
.Lmoepro_done:
	s_add_i32 s0, 0, 0x22540
	v_mov_b32_e32 v0, s0
	s_waitcnt lgkmcnt(0)
	s_barrier
	ds_read_b32 v0, v0
	s_waitcnt lgkmcnt(0)
	v_readfirstlane_b32 s6, v0
	s_cmp_gt_i32 s6, -1
	s_cselect_b64 s[0:1], -1, 0
	s_cmp_lt_i32 s6, 0
	s_cbranch_scc1 .LBB0_703
	s_add_i32 s6, 0, 0x22544
	v_mov_b32_e32 v0, s6
	s_add_i32 s6, 0, 0x2254c
	v_mov_b32_e32 v1, s6
	ds_read_b32 v0, v0
	ds_read_b32 v1, v1
	s_waitcnt lgkmcnt(1)
	v_readfirstlane_b32 s18, v0
	s_waitcnt lgkmcnt(0)
	v_readfirstlane_b32 s19, v1
	s_branch .LBB0_704
